# in-proj phase: tile order permuted so that an XCD owns 17 consecutive row tiles with all 18 column tiles (A rows read by one XCD)
# speedup vs baseline: 1.0257x; 1.0053x over previous
; __global__ void __launch_bounds__(NTHR, 2) mk_fwd(Params prm) {
;     ...
;             case 0: for (int t = bid; t < 136 * 18 + (layer == 0 ? 5120 : 0); t += G) { asm volatile("" : "+v"(c.tid)); if (t < 136 * 18) ph_inproj_mfma(c, layer, t, smem_raw); else ph_prepB(c, t - 136 * 18); } break;
.LBB0_533:
	v_readlane_b32 s60, v254, 4
	s_nop 1
	s_add_i32 s60, s60, s3
	s_cmp_ge_i32 s60, s15
	s_cbranch_scc1 .LBB0_589
.LBB0_534:
	v_writelane_b32 v254, s60, 4
	s_cmpk_gt_i32 s60, 0x98f
	s_cbranch_scc1 .Lip_noperm
	s_and_b32 s0, s60, 7
	s_lshr_b32 s1, s60, 3
	s_mulk_i32 s0, 0x132
	s_add_i32 s60, s0, s1

; #define LAS __attribute__((address_space(3)))
; __device__ __forceinline__ s16x4 lds_tr(lds_cptr p) { return __builtin_bit_cast(s16x4, __builtin_amdgcn_ds_read_tr16_b64_v4i16((LAS s16x4*)p)); }
;     ...
;     auto compute = [&]() __attribute__((always_inline)) {
; #pragma unroll
;         for (int kh = 0; kh < 2; ++kh) {
;             bf16x8 af[4], bfr[4];
; #pragma unroll
;             for (int m = 0; m < 4; ++m) af[m] = *(const LAS bf16x8*)(la + kh * GA_KH + m * 1024);
; #pragma unroll
;             for (int n = 0; n < 4; ++n) {
;                 const s16x4 r0 = lds_tr(lb + kh * 32 * GB_ST + n * 32), r1 = lds_tr(lb + kh * 32 * GB_ST + n * 32 + bsw);
;                 bfr[n] = (bf16x8){r0[0], r0[1], r0[2], r0[3], r1[0], r1[1], r1[2], r1[3]};
;             }
; #pragma unroll
;             for (int m = 0; m < 4; ++m)
; #pragma unroll
;                 for (int n = 0; n < 4; ++n) acc[m][n] = __builtin_amdgcn_mfma_f32_16x16x32_bf16(bfr[n], af[m], acc[m][n], 0, 0, 0);
;         }
;     };
;     ...
;     if (DEEP == 1) {
;         gloadA(0, ra0); gloadB(0, rb0); gloadA(1, ra1);
;         for (int kt = 0; kt < nk; kt += 2) {
;             __syncthreads();
;             lstore(ra0, rb0);
;             __syncthreads();
;             gloadB(kt + 1, rb0);
;             if (kt + 2 < nk) gloadA(kt + 2, ra0);
;             compute();
;             __syncthreads();
;             lstore(ra1, rb0);
;             __syncthreads();
;             if (kt + 2 < nk) gloadB(kt + 2, rb0);
;             if (kt + 3 < nk) gloadA(kt + 3, ra1);
;             compute();
;         }
.Lip_loop:
	s_add_u32 m0, s98, 0x9000
	ds_read_b64_tr_b16 v[158:159], v214 offset:16512
	ds_read_b64_tr_b16 v[160:161], v214 offset:17536
	ds_read_b128 v[128:131], v216
	ds_read_b64_tr_b16 v[162:163], v215 offset:16512
	ds_read_b64_tr_b16 v[164:165], v215 offset:17536
	s_waitcnt lgkmcnt(2)
	v_mfma_f32_16x16x32_bf16 v[64:67], v[158:161], v[128:131], v[64:67]
	global_load_lds_dwordx4 v206, s[44:45]
	s_add_u32 m0, s98, 0xb040
	ds_read_b64_tr_b16 v[166:167], v217 offset:16512
	ds_read_b64_tr_b16 v[168:169], v217 offset:17536
	s_waitcnt lgkmcnt(2)
	v_mfma_f32_16x16x32_bf16 v[60:63], v[162:165], v[128:131], v[60:63]
	global_load_lds_dwordx4 v207, s[44:45]
	s_add_u32 m0, s98, 0x9400
	ds_read_b64_tr_b16 v[170:171], v218 offset:16512
	ds_read_b64_tr_b16 v[172:173], v218 offset:17536
	s_waitcnt lgkmcnt(2)
	v_mfma_f32_16x16x32_bf16 v[56:59], v[166:169], v[128:131], v[56:59]
	global_load_lds_dwordx4 v208, s[44:45]
	s_add_u32 m0, s98, 0xb440
	ds_read_b128 v[132:135], v216 offset:1024
	s_waitcnt lgkmcnt(1)
	v_mfma_f32_16x16x32_bf16 v[52:55], v[170:173], v[128:131], v[52:55]
	global_load_lds_dwordx4 v209, s[44:45]
	s_add_u32 m0, s99, 0xd080
	ds_read_b128 v[136:139], v216 offset:2048
	s_waitcnt lgkmcnt(1)
	v_mfma_f32_16x16x32_bf16 v[48:51], v[158:161], v[132:135], v[48:51]
	global_load_lds_dwordx4 v210, s[46:47]
	s_add_u32 m0, s99, 0xd480
	ds_read_b128 v[140:143], v216 offset:3072
	v_mfma_f32_16x16x32_bf16 v[44:47], v[162:165], v[132:135], v[44:47]
	global_load_lds_dwordx4 v211, s[46:47]
	s_add_u32 m0, s99, 0xd880
	ds_read_b64_tr_b16 v[174:175], v214 offset:24704
	ds_read_b64_tr_b16 v[176:177], v214 offset:25728
	v_mfma_f32_16x16x32_bf16 v[40:43], v[166:169], v[132:135], v[40:43]
	global_load_lds_dwordx4 v212, s[46:47]
	s_add_u32 m0, s99, 0xdc80
	ds_read_b64_tr_b16 v[178:179], v215 offset:24704
	ds_read_b64_tr_b16 v[180:181], v215 offset:25728
	v_mfma_f32_16x16x32_bf16 v[36:39], v[170:173], v[132:135], v[36:39]
	global_load_lds_dwordx4 v213, s[46:47]
	s_add_u32 s44, s44, 0x80
	s_addc_u32 s45, s45, 0
	s_add_u32 s46, s46, 0x48000
	s_addc_u32 s47, s47, 0
	ds_read_b128 v[128:131], v216 offset:8256
	s_waitcnt lgkmcnt(6)
	v_mfma_f32_16x16x32_bf16 v[28:31], v[158:161], v[136:139], v[28:31]
	ds_read_b64_tr_b16 v[182:183], v217 offset:24704
	ds_read_b64_tr_b16 v[184:185], v217 offset:25728
	v_mfma_f32_16x16x32_bf16 v[24:27], v[162:165], v[136:139], v[24:27]
	ds_read_b64_tr_b16 v[186:187], v218 offset:24704
	ds_read_b64_tr_b16 v[188:189], v218 offset:25728
	v_mfma_f32_16x16x32_bf16 v[16:19], v[166:169], v[136:139], v[16:19]
	v_mfma_f32_16x16x32_bf16 v[12:15], v[170:173], v[136:139], v[12:15]
	ds_read_b128 v[132:135], v216 offset:9280
	s_waitcnt lgkmcnt(10)
	v_mfma_f32_16x16x32_bf16 v[8:11], v[158:161], v[140:143], v[8:11]
	v_mfma_f32_16x16x32_bf16 v[4:7], v[162:165], v[140:143], v[4:7]
	v_mfma_f32_16x16x32_bf16 v[32:35], v[166:169], v[140:143], v[32:35]
	v_mfma_f32_16x16x32_bf16 v[20:23], v[170:173], v[140:143], v[20:23]
	ds_read_b128 v[136:139], v216 offset:10304
	s_waitcnt lgkmcnt(6)
	v_mfma_f32_16x16x32_bf16 v[64:67], v[174:177], v[128:131], v[64:67]
	v_mfma_f32_16x16x32_bf16 v[60:63], v[178:181], v[128:131], v[60:63]
	s_waitcnt lgkmcnt(4)
	v_mfma_f32_16x16x32_bf16 v[56:59], v[182:185], v[128:131], v[56:59]
	s_waitcnt lgkmcnt(2)
	v_mfma_f32_16x16x32_bf16 v[52:55], v[186:189], v[128:131], v[52:55]
	ds_read_b128 v[140:143], v216 offset:11328
	s_waitcnt lgkmcnt(2)
	v_mfma_f32_16x16x32_bf16 v[48:51], v[174:177], v[132:135], v[48:51]
	v_mfma_f32_16x16x32_bf16 v[44:47], v[178:181], v[132:135], v[44:47]
	v_mfma_f32_16x16x32_bf16 v[40:43], v[182:185], v[132:135], v[40:43]
	v_mfma_f32_16x16x32_bf16 v[36:39], v[186:189], v[132:135], v[36:39]
	s_waitcnt lgkmcnt(1)
	v_mfma_f32_16x16x32_bf16 v[28:31], v[174:177], v[136:139], v[28:31]
	v_mfma_f32_16x16x32_bf16 v[24:27], v[178:181], v[136:139], v[24:27]
	v_mfma_f32_16x16x32_bf16 v[16:19], v[182:185], v[136:139], v[16:19]
	v_mfma_f32_16x16x32_bf16 v[12:15], v[186:189], v[136:139], v[12:15]
	s_waitcnt lgkmcnt(0)
	v_mfma_f32_16x16x32_bf16 v[8:11], v[174:177], v[140:143], v[8:11]
	v_mfma_f32_16x16x32_bf16 v[4:7], v[178:181], v[140:143], v[4:7]
	v_mfma_f32_16x16x32_bf16 v[32:35], v[182:185], v[140:143], v[32:35]
	v_mfma_f32_16x16x32_bf16 v[20:23], v[186:189], v[140:143], v[20:23]
	s_waitcnt vmcnt(0) lgkmcnt(0)
	s_barrier
; #define LAS __attribute__((address_space(3)))
; __device__ __forceinline__ s16x4 lds_tr(lds_cptr p) { return __builtin_bit_cast(s16x4, __builtin_amdgcn_ds_read_tr16_b64_v4i16((LAS s16x4*)p)); }
;     ...
;     auto compute = [&]() __attribute__((always_inline)) {
; #pragma unroll
;         for (int kh = 0; kh < 2; ++kh) {
;             bf16x8 af[4], bfr[4];
; #pragma unroll
;             for (int m = 0; m < 4; ++m) af[m] = *(const LAS bf16x8*)(la + kh * GA_KH + m * 1024);
; #pragma unroll
;             for (int n = 0; n < 4; ++n) {
;                 const s16x4 r0 = lds_tr(lb + kh * 32 * GB_ST + n * 32), r1 = lds_tr(lb + kh * 32 * GB_ST + n * 32 + bsw);
;                 bfr[n] = (bf16x8){r0[0], r0[1], r0[2], r0[3], r1[0], r1[1], r1[2], r1[3]};
;             }
; #pragma unroll
;             for (int m = 0; m < 4; ++m)
; #pragma unroll
;                 for (int n = 0; n < 4; ++n) acc[m][n] = __builtin_amdgcn_mfma_f32_16x16x32_bf16(bfr[n], af[m], acc[m][n], 0, 0, 0);
;         }
;     };
;     ...
;     if (DEEP == 1) {
;         gloadA(0, ra0); gloadB(0, rb0); gloadA(1, ra1);
;         for (int kt = 0; kt < nk; kt += 2) {
;             __syncthreads();
;             lstore(ra0, rb0);
;             __syncthreads();
;             gloadB(kt + 1, rb0);
;             if (kt + 2 < nk) gloadA(kt + 2, ra0);
;             compute();
;             __syncthreads();
;             lstore(ra1, rb0);
;             __syncthreads();
;             if (kt + 2 < nk) gloadB(kt + 2, rb0);
;             if (kt + 3 < nk) gloadA(kt + 3, ra1);
;             compute();
;         }
	s_add_u32 m0, s98, 0x0
	ds_read_b64_tr_b16 v[158:159], v214 offset:53376
	ds_read_b64_tr_b16 v[160:161], v214 offset:54400
	ds_read_b128 v[128:131], v216 offset:36864
	ds_read_b64_tr_b16 v[162:163], v215 offset:53376
	ds_read_b64_tr_b16 v[164:165], v215 offset:54400
	s_waitcnt lgkmcnt(2)
	v_mfma_f32_16x16x32_bf16 v[64:67], v[158:161], v[128:131], v[64:67]
	global_load_lds_dwordx4 v206, s[44:45]
	s_add_u32 m0, s98, 0x2040
	ds_read_b64_tr_b16 v[166:167], v217 offset:53376
	ds_read_b64_tr_b16 v[168:169], v217 offset:54400
	s_waitcnt lgkmcnt(2)
	v_mfma_f32_16x16x32_bf16 v[60:63], v[162:165], v[128:131], v[60:63]
	global_load_lds_dwordx4 v207, s[44:45]
	s_add_u32 m0, s98, 0x400
	ds_read_b64_tr_b16 v[170:171], v218 offset:53376
	ds_read_b64_tr_b16 v[172:173], v218 offset:54400
	s_waitcnt lgkmcnt(2)
	v_mfma_f32_16x16x32_bf16 v[56:59], v[166:169], v[128:131], v[56:59]
	global_load_lds_dwordx4 v208, s[44:45]
	s_add_u32 m0, s98, 0x2440
	ds_read_b128 v[132:135], v216 offset:37888
	s_waitcnt lgkmcnt(1)
	v_mfma_f32_16x16x32_bf16 v[52:55], v[170:173], v[128:131], v[52:55]
	global_load_lds_dwordx4 v209, s[44:45]
	s_add_u32 m0, s99, 0x4080
	ds_read_b128 v[136:139], v216 offset:38912
	s_waitcnt lgkmcnt(1)
	v_mfma_f32_16x16x32_bf16 v[48:51], v[158:161], v[132:135], v[48:51]
	global_load_lds_dwordx4 v210, s[46:47]
	s_add_u32 m0, s99, 0x4480
	ds_read_b128 v[140:143], v216 offset:39936
	v_mfma_f32_16x16x32_bf16 v[44:47], v[162:165], v[132:135], v[44:47]
	global_load_lds_dwordx4 v211, s[46:47]
	s_add_u32 m0, s99, 0x4880
	ds_read_b64_tr_b16 v[174:175], v214 offset:61568
	ds_read_b64_tr_b16 v[176:177], v214 offset:62592
	v_mfma_f32_16x16x32_bf16 v[40:43], v[166:169], v[132:135], v[40:43]
	global_load_lds_dwordx4 v212, s[46:47]
	s_add_u32 m0, s99, 0x4c80
	ds_read_b64_tr_b16 v[178:179], v215 offset:61568
	ds_read_b64_tr_b16 v[180:181], v215 offset:62592
	v_mfma_f32_16x16x32_bf16 v[36:39], v[170:173], v[132:135], v[36:39]
	global_load_lds_dwordx4 v213, s[46:47]
	s_add_u32 s44, s44, 0x80
	s_addc_u32 s45, s45, 0
	s_add_u32 s46, s46, 0x48000
	s_addc_u32 s47, s47, 0
	ds_read_b128 v[128:131], v216 offset:45120
	s_waitcnt lgkmcnt(6)
	v_mfma_f32_16x16x32_bf16 v[28:31], v[158:161], v[136:139], v[28:31]
	ds_read_b64_tr_b16 v[182:183], v217 offset:61568
	ds_read_b64_tr_b16 v[184:185], v217 offset:62592
	v_mfma_f32_16x16x32_bf16 v[24:27], v[162:165], v[136:139], v[24:27]
	ds_read_b64_tr_b16 v[186:187], v218 offset:61568
	ds_read_b64_tr_b16 v[188:189], v218 offset:62592
	v_mfma_f32_16x16x32_bf16 v[16:19], v[166:169], v[136:139], v[16:19]
	v_mfma_f32_16x16x32_bf16 v[12:15], v[170:173], v[136:139], v[12:15]
	ds_read_b128 v[132:135], v216 offset:46144
	s_waitcnt lgkmcnt(10)
	v_mfma_f32_16x16x32_bf16 v[8:11], v[158:161], v[140:143], v[8:11]
	v_mfma_f32_16x16x32_bf16 v[4:7], v[162:165], v[140:143], v[4:7]
	v_mfma_f32_16x16x32_bf16 v[32:35], v[166:169], v[140:143], v[32:35]
	v_mfma_f32_16x16x32_bf16 v[20:23], v[170:173], v[140:143], v[20:23]
	ds_read_b128 v[136:139], v216 offset:47168
	s_waitcnt lgkmcnt(6)
	v_mfma_f32_16x16x32_bf16 v[64:67], v[174:177], v[128:131], v[64:67]
	v_mfma_f32_16x16x32_bf16 v[60:63], v[178:181], v[128:131], v[60:63]
	s_waitcnt lgkmcnt(4)
	v_mfma_f32_16x16x32_bf16 v[56:59], v[182:185], v[128:131], v[56:59]
	s_waitcnt lgkmcnt(2)
	v_mfma_f32_16x16x32_bf16 v[52:55], v[186:189], v[128:131], v[52:55]
	ds_read_b128 v[140:143], v216 offset:48192
	s_waitcnt lgkmcnt(2)
	v_mfma_f32_16x16x32_bf16 v[48:51], v[174:177], v[132:135], v[48:51]
	v_mfma_f32_16x16x32_bf16 v[44:47], v[178:181], v[132:135], v[44:47]
	v_mfma_f32_16x16x32_bf16 v[40:43], v[182:185], v[132:135], v[40:43]
	v_mfma_f32_16x16x32_bf16 v[36:39], v[186:189], v[132:135], v[36:39]
	s_waitcnt lgkmcnt(1)
	v_mfma_f32_16x16x32_bf16 v[28:31], v[174:177], v[136:139], v[28:31]
	v_mfma_f32_16x16x32_bf16 v[24:27], v[178:181], v[136:139], v[24:27]
	v_mfma_f32_16x16x32_bf16 v[16:19], v[182:185], v[136:139], v[16:19]
	v_mfma_f32_16x16x32_bf16 v[12:15], v[186:189], v[136:139], v[12:15]
	s_waitcnt lgkmcnt(0)
	v_mfma_f32_16x16x32_bf16 v[8:11], v[174:177], v[140:143], v[8:11]
	v_mfma_f32_16x16x32_bf16 v[4:7], v[178:181], v[140:143], v[4:7]
	v_mfma_f32_16x16x32_bf16 v[32:35], v[182:185], v[140:143], v[32:35]
	v_mfma_f32_16x16x32_bf16 v[20:23], v[186:189], v[140:143], v[20:23]
	s_waitcnt vmcnt(0) lgkmcnt(0)
	s_barrier
	s_add_i32 s6, s6, 2
	s_cmp_lt_u32 s6, 14
	s_cbranch_scc1 .Lip_loop
; #define LAS __attribute__((address_space(3)))
; __device__ __forceinline__ s16x4 lds_tr(lds_cptr p) { return __builtin_bit_cast(s16x4, __builtin_amdgcn_ds_read_tr16_b64_v4i16((LAS s16x4*)p)); }
;     ...
;     auto compute = [&]() __attribute__((always_inline)) {
; #pragma unroll
;         for (int kh = 0; kh < 2; ++kh) {
;             bf16x8 af[4], bfr[4];
; #pragma unroll
;             for (int m = 0; m < 4; ++m) af[m] = *(const LAS bf16x8*)(la + kh * GA_KH + m * 1024);
; #pragma unroll
;             for (int n = 0; n < 4; ++n) {
;                 const s16x4 r0 = lds_tr(lb + kh * 32 * GB_ST + n * 32), r1 = lds_tr(lb + kh * 32 * GB_ST + n * 32 + bsw);
;                 bfr[n] = (bf16x8){r0[0], r0[1], r0[2], r0[3], r1[0], r1[1], r1[2], r1[3]};
;             }
; #pragma unroll
;             for (int m = 0; m < 4; ++m)
; #pragma unroll
;                 for (int n = 0; n < 4; ++n) acc[m][n] = __builtin_amdgcn_mfma_f32_16x16x32_bf16(bfr[n], af[m], acc[m][n], 0, 0, 0);
;         }
;     };
;     ...
;     if (DEEP == 1) {
;         gloadA(0, ra0); gloadB(0, rb0); gloadA(1, ra1);
;         for (int kt = 0; kt < nk; kt += 2) {
;             __syncthreads();
;             lstore(ra0, rb0);
;             __syncthreads();
;             gloadB(kt + 1, rb0);
;             if (kt + 2 < nk) gloadA(kt + 2, ra0);
;             compute();
;             __syncthreads();
;             lstore(ra1, rb0);
;             __syncthreads();
;             if (kt + 2 < nk) gloadB(kt + 2, rb0);
;             if (kt + 3 < nk) gloadA(kt + 3, ra1);
;             compute();
;         }
	s_add_u32 m0, s98, 0x9000
	ds_read_b64_tr_b16 v[158:159], v214 offset:16512
	ds_read_b64_tr_b16 v[160:161], v214 offset:17536
	ds_read_b128 v[128:131], v216
	ds_read_b64_tr_b16 v[162:163], v215 offset:16512
	ds_read_b64_tr_b16 v[164:165], v215 offset:17536
	s_waitcnt lgkmcnt(2)
	v_mfma_f32_16x16x32_bf16 v[64:67], v[158:161], v[128:131], v[64:67]
	global_load_lds_dwordx4 v206, s[44:45]
	s_add_u32 m0, s98, 0xb040
	ds_read_b64_tr_b16 v[166:167], v217 offset:16512
	ds_read_b64_tr_b16 v[168:169], v217 offset:17536
	s_waitcnt lgkmcnt(2)
	v_mfma_f32_16x16x32_bf16 v[60:63], v[162:165], v[128:131], v[60:63]
	global_load_lds_dwordx4 v207, s[44:45]
	s_add_u32 m0, s98, 0x9400
	ds_read_b64_tr_b16 v[170:171], v218 offset:16512
	ds_read_b64_tr_b16 v[172:173], v218 offset:17536
	s_waitcnt lgkmcnt(2)
	v_mfma_f32_16x16x32_bf16 v[56:59], v[166:169], v[128:131], v[56:59]
	global_load_lds_dwordx4 v208, s[44:45]
	s_add_u32 m0, s98, 0xb440
	ds_read_b128 v[132:135], v216 offset:1024
	s_waitcnt lgkmcnt(1)
	v_mfma_f32_16x16x32_bf16 v[52:55], v[170:173], v[128:131], v[52:55]
	global_load_lds_dwordx4 v209, s[44:45]
	s_add_u32 m0, s99, 0xd080
	ds_read_b128 v[136:139], v216 offset:2048
	s_waitcnt lgkmcnt(1)
	v_mfma_f32_16x16x32_bf16 v[48:51], v[158:161], v[132:135], v[48:51]
	global_load_lds_dwordx4 v210, s[46:47]
	s_add_u32 m0, s99, 0xd480
	ds_read_b128 v[140:143], v216 offset:3072
	v_mfma_f32_16x16x32_bf16 v[44:47], v[162:165], v[132:135], v[44:47]
	global_load_lds_dwordx4 v211, s[46:47]
	s_add_u32 m0, s99, 0xd880
	ds_read_b64_tr_b16 v[174:175], v214 offset:24704
	ds_read_b64_tr_b16 v[176:177], v214 offset:25728
	v_mfma_f32_16x16x32_bf16 v[40:43], v[166:169], v[132:135], v[40:43]
	global_load_lds_dwordx4 v212, s[46:47]
	s_add_u32 m0, s99, 0xdc80
	ds_read_b64_tr_b16 v[178:179], v215 offset:24704
	ds_read_b64_tr_b16 v[180:181], v215 offset:25728
	v_mfma_f32_16x16x32_bf16 v[36:39], v[170:173], v[132:135], v[36:39]
	global_load_lds_dwordx4 v213, s[46:47]
	s_add_u32 s44, s44, 0x80
	s_addc_u32 s45, s45, 0
	s_add_u32 s46, s46, 0x48000
	s_addc_u32 s47, s47, 0
	ds_read_b128 v[128:131], v216 offset:8256
	s_waitcnt lgkmcnt(6)
	v_mfma_f32_16x16x32_bf16 v[28:31], v[158:161], v[136:139], v[28:31]
	ds_read_b64_tr_b16 v[182:183], v217 offset:24704
	ds_read_b64_tr_b16 v[184:185], v217 offset:25728
	v_mfma_f32_16x16x32_bf16 v[24:27], v[162:165], v[136:139], v[24:27]
	ds_read_b64_tr_b16 v[186:187], v218 offset:24704
	ds_read_b64_tr_b16 v[188:189], v218 offset:25728
	v_mfma_f32_16x16x32_bf16 v[16:19], v[166:169], v[136:139], v[16:19]
	v_mfma_f32_16x16x32_bf16 v[12:15], v[170:173], v[136:139], v[12:15]
	ds_read_b128 v[132:135], v216 offset:9280
	s_waitcnt lgkmcnt(10)
	v_mfma_f32_16x16x32_bf16 v[8:11], v[158:161], v[140:143], v[8:11]
	v_mfma_f32_16x16x32_bf16 v[4:7], v[162:165], v[140:143], v[4:7]
	v_mfma_f32_16x16x32_bf16 v[32:35], v[166:169], v[140:143], v[32:35]
	v_mfma_f32_16x16x32_bf16 v[20:23], v[170:173], v[140:143], v[20:23]
	ds_read_b128 v[136:139], v216 offset:10304
	s_waitcnt lgkmcnt(6)
	v_mfma_f32_16x16x32_bf16 v[64:67], v[174:177], v[128:131], v[64:67]
	v_mfma_f32_16x16x32_bf16 v[60:63], v[178:181], v[128:131], v[60:63]
	s_waitcnt lgkmcnt(4)
	v_mfma_f32_16x16x32_bf16 v[56:59], v[182:185], v[128:131], v[56:59]
	s_waitcnt lgkmcnt(2)
	v_mfma_f32_16x16x32_bf16 v[52:55], v[186:189], v[128:131], v[52:55]
	ds_read_b128 v[140:143], v216 offset:11328
	s_waitcnt lgkmcnt(2)
	v_mfma_f32_16x16x32_bf16 v[48:51], v[174:177], v[132:135], v[48:51]
	v_mfma_f32_16x16x32_bf16 v[44:47], v[178:181], v[132:135], v[44:47]
	v_mfma_f32_16x16x32_bf16 v[40:43], v[182:185], v[132:135], v[40:43]
	v_mfma_f32_16x16x32_bf16 v[36:39], v[186:189], v[132:135], v[36:39]
	s_waitcnt lgkmcnt(1)
	v_mfma_f32_16x16x32_bf16 v[28:31], v[174:177], v[136:139], v[28:31]
	v_mfma_f32_16x16x32_bf16 v[24:27], v[178:181], v[136:139], v[24:27]
	v_mfma_f32_16x16x32_bf16 v[16:19], v[182:185], v[136:139], v[16:19]
	v_mfma_f32_16x16x32_bf16 v[12:15], v[186:189], v[136:139], v[12:15]
	s_waitcnt lgkmcnt(0)
	v_mfma_f32_16x16x32_bf16 v[8:11], v[174:177], v[140:143], v[8:11]
	v_mfma_f32_16x16x32_bf16 v[4:7], v[178:181], v[140:143], v[4:7]
	v_mfma_f32_16x16x32_bf16 v[32:35], v[182:185], v[140:143], v[32:35]
	v_mfma_f32_16x16x32_bf16 v[20:23], v[186:189], v[140:143], v[20:23]
	s_waitcnt vmcnt(0) lgkmcnt(0)
	s_barrier
; #define LAS __attribute__((address_space(3)))
;     template <class T> __device__ __forceinline__ T* w(size_t off) const { return (T*)(p->ws + off); }
; __device__ __forceinline__ s16x4 lds_tr(lds_cptr p) { return __builtin_bit_cast(s16x4, __builtin_amdgcn_ds_read_tr16_b64_v4i16((LAS s16x4*)p)); }
;     ...
;     auto compute = [&]() __attribute__((always_inline)) {
; #pragma unroll
;         for (int kh = 0; kh < 2; ++kh) {
;             bf16x8 af[4], bfr[4];
; #pragma unroll
;             for (int m = 0; m < 4; ++m) af[m] = *(const LAS bf16x8*)(la + kh * GA_KH + m * 1024);
; #pragma unroll
;             for (int n = 0; n < 4; ++n) {
;                 const s16x4 r0 = lds_tr(lb + kh * 32 * GB_ST + n * 32), r1 = lds_tr(lb + kh * 32 * GB_ST + n * 32 + bsw);
;                 bfr[n] = (bf16x8){r0[0], r0[1], r0[2], r0[3], r1[0], r1[1], r1[2], r1[3]};
;             }
; #pragma unroll
;             for (int m = 0; m < 4; ++m)
; #pragma unroll
;                 for (int n = 0; n < 4; ++n) acc[m][n] = __builtin_amdgcn_mfma_f32_16x16x32_bf16(bfr[n], af[m], acc[m][n], 0, 0, 0);
;         }
;     };
; __device__ __forceinline__ void ph_inproj_mfma(const Ctx& c, int layer, int tile, unsigned char* lds) {
;     const int mt = tile / 18, nt = tile % 18;
;     const bf16* HA = c.w<bf16>(WS_HA) + (size_t)mt * 128 * D;
;     f32x4 acc[4][4];
;     const int vc = nt * 128 + (c.tid & 15) * 8;
;     gemm_tile<false, 1>(c.tid, lds, HA, [&](int r) __attribute__((always_inline)) { return (unsigned)(r * D); }, c.w<bf16>(WS_BIN) + (size_t)layer * D * DINV, (unsigned)vc, DINV, true, D, acc);
	ds_read_b64_tr_b16 v[158:159], v214 offset:53376
	ds_read_b64_tr_b16 v[160:161], v214 offset:54400
	ds_read_b128 v[128:131], v216 offset:36864
	ds_read_b64_tr_b16 v[162:163], v215 offset:53376
	ds_read_b64_tr_b16 v[164:165], v215 offset:54400
	s_waitcnt lgkmcnt(2)
	v_mfma_f32_16x16x32_bf16 v[64:67], v[158:161], v[128:131], v[64:67]
	ds_read_b64_tr_b16 v[166:167], v217 offset:53376
	ds_read_b64_tr_b16 v[168:169], v217 offset:54400
	s_waitcnt lgkmcnt(2)
	v_mfma_f32_16x16x32_bf16 v[60:63], v[162:165], v[128:131], v[60:63]
	ds_read_b64_tr_b16 v[170:171], v218 offset:53376
	ds_read_b64_tr_b16 v[172:173], v218 offset:54400
	s_waitcnt lgkmcnt(2)
	v_mfma_f32_16x16x32_bf16 v[56:59], v[166:169], v[128:131], v[56:59]
	ds_read_b128 v[132:135], v216 offset:37888
	s_waitcnt lgkmcnt(1)
	v_mfma_f32_16x16x32_bf16 v[52:55], v[170:173], v[128:131], v[52:55]
	ds_read_b128 v[136:139], v216 offset:38912
	s_waitcnt lgkmcnt(1)
	v_mfma_f32_16x16x32_bf16 v[48:51], v[158:161], v[132:135], v[48:51]
	ds_read_b128 v[140:143], v216 offset:39936
	v_mfma_f32_16x16x32_bf16 v[44:47], v[162:165], v[132:135], v[44:47]
	ds_read_b64_tr_b16 v[174:175], v214 offset:61568
	ds_read_b64_tr_b16 v[176:177], v214 offset:62592
	v_mfma_f32_16x16x32_bf16 v[40:43], v[166:169], v[132:135], v[40:43]
	ds_read_b64_tr_b16 v[178:179], v215 offset:61568
	ds_read_b64_tr_b16 v[180:181], v215 offset:62592
	v_mfma_f32_16x16x32_bf16 v[36:39], v[170:173], v[132:135], v[36:39]
	ds_read_b128 v[128:131], v216 offset:45120
	s_waitcnt lgkmcnt(6)
	v_mfma_f32_16x16x32_bf16 v[28:31], v[158:161], v[136:139], v[28:31]
	ds_read_b64_tr_b16 v[182:183], v217 offset:61568
	ds_read_b64_tr_b16 v[184:185], v217 offset:62592
	v_mfma_f32_16x16x32_bf16 v[24:27], v[162:165], v[136:139], v[24:27]
	ds_read_b64_tr_b16 v[186:187], v218 offset:61568
	ds_read_b64_tr_b16 v[188:189], v218 offset:62592
	v_mfma_f32_16x16x32_bf16 v[16:19], v[166:169], v[136:139], v[16:19]
	v_mfma_f32_16x16x32_bf16 v[12:15], v[170:173], v[136:139], v[12:15]
	ds_read_b128 v[132:135], v216 offset:46144
	s_waitcnt lgkmcnt(10)
	v_mfma_f32_16x16x32_bf16 v[8:11], v[158:161], v[140:143], v[8:11]
	v_mfma_f32_16x16x32_bf16 v[4:7], v[162:165], v[140:143], v[4:7]
	v_mfma_f32_16x16x32_bf16 v[32:35], v[166:169], v[140:143], v[32:35]
	v_mfma_f32_16x16x32_bf16 v[20:23], v[170:173], v[140:143], v[20:23]
	ds_read_b128 v[136:139], v216 offset:47168
	s_waitcnt lgkmcnt(6)
	v_mfma_f32_16x16x32_bf16 v[64:67], v[174:177], v[128:131], v[64:67]
	v_mfma_f32_16x16x32_bf16 v[60:63], v[178:181], v[128:131], v[60:63]
	s_waitcnt lgkmcnt(4)
	v_mfma_f32_16x16x32_bf16 v[56:59], v[182:185], v[128:131], v[56:59]
	s_waitcnt lgkmcnt(2)
	v_mfma_f32_16x16x32_bf16 v[52:55], v[186:189], v[128:131], v[52:55]
	ds_read_b128 v[140:143], v216 offset:48192
	s_waitcnt lgkmcnt(2)
	v_mfma_f32_16x16x32_bf16 v[48:51], v[174:177], v[132:135], v[48:51]
	v_mfma_f32_16x16x32_bf16 v[44:47], v[178:181], v[132:135], v[44:47]
	v_mfma_f32_16x16x32_bf16 v[40:43], v[182:185], v[132:135], v[40:43]
	v_mfma_f32_16x16x32_bf16 v[36:39], v[186:189], v[132:135], v[36:39]
	s_waitcnt lgkmcnt(1)
	v_mfma_f32_16x16x32_bf16 v[28:31], v[174:177], v[136:139], v[28:31]
	v_mfma_f32_16x16x32_bf16 v[24:27], v[178:181], v[136:139], v[24:27]
	v_mfma_f32_16x16x32_bf16 v[16:19], v[182:185], v[136:139], v[16:19]
	v_mfma_f32_16x16x32_bf16 v[12:15], v[186:189], v[136:139], v[12:15]
	s_waitcnt lgkmcnt(0)
	v_mfma_f32_16x16x32_bf16 v[8:11], v[174:177], v[140:143], v[8:11]
	v_mfma_f32_16x16x32_bf16 v[4:7], v[178:181], v[140:143], v[4:7]
	v_mfma_f32_16x16x32_bf16 v[32:35], v[182:185], v[140:143], v[32:35]
	v_mfma_f32_16x16x32_bf16 v[20:23], v[186:189], v[140:143], v[20:23]
	s_waitcnt vmcnt(0) lgkmcnt(0)
	s_barrier
	v_readlane_b32 s6, v254, 4
	s_nop 1
	s_add_i32 s6, s6, s3
	s_cmpk_gt_i32 s6, 0x98f
	s_cbranch_scc1 .Lip_nopf
	s_and_b32 s100, s6, 7
	s_lshr_b32 s6, s6, 3
	s_mulk_i32 s100, 0x132
	s_add_i32 s6, s6, s100
	s_mul_hi_i32 s100, s6, 0x38e38e39
	s_lshr_b32 s101, s100, 31
	s_ashr_i32 s100, s100, 2
	s_add_i32 s100, s100, s101
	s_mul_i32 s101, s100, 18
	s_sub_i32 s6, s6, s101
	s_lshl_b32 s6, s6, 8
	s_ashr_i32 s101, s100, 31
	s_lshl_b64 s[100:101], s[100:101], 18
	s_add_u32 s100, s42, s100
	s_addc_u32 s101, s43, s101
	s_add_u32 s100, s100, 0x45c6000
	s_addc_u32 s101, s101, 0
	s_add_u32 m0, s98, 0x0
	s_nop 0
	global_load_lds_dwordx4 v206, s[100:101]
	s_add_u32 m0, s98, 0x2040
	s_nop 0
	global_load_lds_dwordx4 v207, s[100:101]
	s_add_u32 m0, s98, 0x400
	s_nop 0
	global_load_lds_dwordx4 v208, s[100:101]
	s_add_u32 m0, s98, 0x2440
	s_nop 0
	global_load_lds_dwordx4 v209, s[100:101]
	s_add_u32 s100, s42, s59
	s_addc_u32 s101, s43, s58
	s_add_u32 s100, s100, 0x18095100
	s_addc_u32 s101, s101, 0
	s_add_u32 s100, s100, s6
	s_addc_u32 s101, s101, 0
	s_add_u32 m0, s99, 0x4080
	s_nop 0
	global_load_lds_dwordx4 v210, s[100:101]
	s_add_u32 m0, s99, 0x4480
	s_nop 0
	global_load_lds_dwordx4 v211, s[100:101]
	s_add_u32 m0, s99, 0x4880
	s_nop 0
	global_load_lds_dwordx4 v212, s[100:101]
	s_add_u32 m0, s99, 0x4c80
	s_nop 0
	global_load_lds_dwordx4 v213, s[100:101]
	s_mov_b32 s101, 1
	s_branch .Lip_pfdone
